# batched barrier-census loads, x1 un-sum LDS reads and PanelRms slot loads (serial round trips removed)
# speedup vs baseline: 1.0047x; 1.0047x over previous
;     __device__ __forceinline__ bool run(const f32x4 (&v)[2][2][4][2], const Unit& u, int wr, int wc, int fr, int fq, PG8_LAS unsigned char* lds, int wid, int lane) const {
;     ...
;         if (lane < 32) {
;             const float* sl = slots + (size_t)(u.pm * BM + row) * 4; float tot = 0.f;
; #pragma unroll
;             for (int t = 0; t < 4; ++t) tot += __hip_atomic_load(sl + t, __ATOMIC_RELAXED, __HIP_MEMORY_SCOPE_AGENT);
;             S[row] = rsqrtf(tot * (1.f / 1024.f) + RMS_EPS);
.LBB0_190:
	s_waitcnt vmcnt(0) lgkmcnt(0)
	s_barrier
	ds_read_b32 v116, v97 offset:5120
	s_and_saveexec_b64 s[2:3], s[0:1]
	s_cbranch_execz .LBB0_192
	v_readlane_b32 s0, v253, 29
	v_readlane_b32 s1, v253, 30
	s_nop 1
	v_lshl_add_u64 v[0:1], v[0:1], 4, s[0:1]
	global_load_dword v3, v[0:1], off sc1
	global_load_dword v4, v[0:1], off offset:4 sc1
	global_load_dword v5, v[0:1], off offset:8 sc1
	global_load_dword v6, v[0:1], off offset:12 sc1
	s_waitcnt vmcnt(3)
	v_add_f32_e32 v3, 0, v3
	s_waitcnt vmcnt(2)
	v_add_f32_e32 v3, v3, v4
	s_waitcnt vmcnt(1)
	v_add_f32_e32 v3, v3, v5
	s_waitcnt vmcnt(0)
	v_add_f32_e32 v0, v3, v6
	v_fmamk_f32 v0, v0, 0x3a800000, v242
	v_cmp_gt_f32_e32 vcc, s44, v0
	v_mul_f32_e32 v1, 0x4b800000, v0
	s_nop 0
	v_cndmask_b32_e32 v0, v0, v1, vcc
	v_rsq_f32_e32 v0, v0
	s_nop 0
	v_mul_f32_e32 v1, 0x45800000, v0
	v_cndmask_b32_e32 v0, v0, v1, vcc
	v_lshl_add_u32 v1, v2, 2, 0
	ds_write_b32 v1, v0 offset:4096

;     __device__ __forceinline__ bool run(const f32x4 (&v)[2][2][4][2], const Unit& u, int wr, int wc, int fr, int fq, PG8_LAS unsigned char* lds, int wid, int lane) const {
;     ...
;         if (lane < 32) {
;             const float* sl = slots + (size_t)(u.pm * BM + row) * 4; float tot = 0.f;
; #pragma unroll
;             for (int t = 0; t < 4; ++t) tot += __hip_atomic_load(sl + t, __ATOMIC_RELAXED, __HIP_MEMORY_SCOPE_AGENT);
;             S[row] = rsqrtf(tot * (1.f / 1024.f) + RMS_EPS);
.LBB0_269:
	s_waitcnt vmcnt(0) lgkmcnt(0)
	s_barrier
	ds_read_b32 v148, v97 offset:5120
	s_and_saveexec_b64 s[2:3], s[0:1]
	s_cbranch_execz .LBB0_271
	v_readlane_b32 s0, v253, 29
	v_readlane_b32 s1, v253, 30
	s_nop 1
	v_lshl_add_u64 v[130:131], v[130:131], 4, s[0:1]
	global_load_dword v133, v[130:131], off sc1
	global_load_dword v134, v[130:131], off offset:4 sc1
	global_load_dword v135, v[130:131], off offset:8 sc1
	global_load_dword v136, v[130:131], off offset:12 sc1
	s_waitcnt vmcnt(3)
	v_add_f32_e32 v133, 0, v133
	s_waitcnt vmcnt(2)
	v_add_f32_e32 v133, v133, v134
	s_waitcnt vmcnt(1)
	v_add_f32_e32 v133, v133, v135
	s_waitcnt vmcnt(0)
	v_add_f32_e32 v130, v133, v136
	v_fmamk_f32 v130, v130, 0x3a800000, v242
	v_cmp_gt_f32_e32 vcc, s44, v130
	v_mul_f32_e32 v131, 0x4b800000, v130
	s_nop 0
	v_cndmask_b32_e32 v130, v130, v131, vcc
	v_rsq_f32_e32 v130, v130
	s_nop 0
	v_mul_f32_e32 v131, 0x45800000, v130
	v_cndmask_b32_e32 v130, v130, v131, vcc
	v_lshl_add_u32 v131, v132, 2, 0
	ds_write_b32 v131, v130 offset:4096
